# expert-sort gather: non-temporal hint on the 16 read-once source loads (on top of the combine-phase hint)
# baseline (speedup 1.0000x reference)
.LBB0_1459:
	v_readlane_b32 s0, v251, 28
	s_lshl_b32 s2, s0, 3
	s_add_i32 s0, s2, s10
	v_lshlrev_b32_e32 v2, 4, v1
	s_ashr_i32 s1, s0, 31
	v_lshl_add_u64 v[4:5], s[24:25], 0, v[2:3]
	s_lshl_b64 s[4:5], s[0:1], 11
	s_waitcnt vmcnt(11)
	v_lshl_add_u64 v[18:19], v[4:5], 0, s[4:5]
	s_waitcnt lgkmcnt(0)
	s_barrier
	s_mov_b32 s98, 0x1000
	s_mov_b32 s99, 0
	v_lshl_add_u64 v[128:129], v[18:19], 0, s[98:99]
	s_mov_b32 s98, 0x2000
	s_mov_b32 s99, 0
	v_lshl_add_u64 v[130:131], v[18:19], 0, s[98:99]
	s_mov_b32 s98, 0x3000
	s_mov_b32 s99, 0
	v_lshl_add_u64 v[132:133], v[18:19], 0, s[98:99]
	global_load_dwordx4 v[64:67], v[18:19], off nt
	global_load_dwordx4 v[68:71], v[18:19], off offset:1024 nt
	global_load_dwordx4 v[72:75], v[18:19], off offset:2048 nt
	global_load_dwordx4 v[76:79], v[18:19], off offset:3072 nt
	global_load_dwordx4 v[80:83], v[128:129], off nt
	global_load_dwordx4 v[84:87], v[128:129], off offset:1024 nt
	global_load_dwordx4 v[88:91], v[128:129], off offset:2048 nt
	global_load_dwordx4 v[92:95], v[128:129], off offset:3072 nt
	global_load_dwordx4 v[96:99], v[130:131], off nt
	global_load_dwordx4 v[100:103], v[130:131], off offset:1024 nt
	global_load_dwordx4 v[104:107], v[130:131], off offset:2048 nt
	global_load_dwordx4 v[108:111], v[130:131], off offset:3072 nt
	global_load_dwordx4 v[112:115], v[132:133], off nt
	global_load_dwordx4 v[116:119], v[132:133], off offset:1024 nt
	global_load_dwordx4 v[120:123], v[132:133], off offset:2048 nt
	global_load_dwordx4 v[124:127], v[132:133], off offset:3072 nt
	v_readlane_b32 s1, v251, 27
	s_andn2_b32 s1, s1, 63
	s_add_i32 s1, s1, 0
	v_mov_b32_e32 v10, s1
	ds_read_b128 v[10:13], v10 offset:8320
	s_or_b32 s3, s2, 2
	s_lshl_b32 s1, s3, 3
	s_add_i32 s1, s1, 0
	v_mov_b32_e32 v14, s1
	ds_read_b128 v[14:17], v14 offset:8320
	s_waitcnt lgkmcnt(1)
	v_ashrrev_i32_e32 v21, 31, v10
	v_mov_b32_e32 v20, v10
	v_lshl_add_u64 v[2:3], s[26:27], 0, v[2:3]
	s_waitcnt vmcnt(11)
	v_ashrrev_i32_e32 v23, 31, v11
	v_mov_b32_e32 v22, v11
	v_lshlrev_b64 v[20:21], 11, v[20:21]
	v_lshlrev_b64 v[10:11], 11, v[22:23]
	v_lshl_add_u64 v[20:21], v[2:3], 0, v[20:21]
	v_lshl_add_u64 v[10:11], v[2:3], 0, v[10:11]
	s_add_i32 s4, s0, 1
	s_ashr_i32 s5, s4, 31
	s_lshl_b64 s[4:5], s[4:5], 11
	s_or_b32 s1, s2, 4
	s_waitcnt vmcnt(15)
	global_store_dwordx4 v[20:21], v[64:67], off
	global_store_dwordx4 v[10:11], v[64:67], off
	v_lshl_add_u64 v[18:19], v[4:5], 0, s[4:5]
	s_add_i32 s4, s3, s10
	s_ashr_i32 s5, s4, 31
	s_lshl_b64 s[4:5], s[4:5], 11
	s_waitcnt vmcnt(16)
	global_store_dwordx4 v[20:21], v[68:71], off offset:1024
	global_store_dwordx4 v[10:11], v[68:71], off offset:1024
	v_ashrrev_i32_e32 v11, 31, v12
	v_mov_b32_e32 v10, v12
	v_ashrrev_i32_e32 v21, 31, v13
	v_mov_b32_e32 v20, v13
	v_lshlrev_b64 v[10:11], 11, v[10:11]
	v_lshlrev_b64 v[12:13], 11, v[20:21]
	v_lshl_add_u64 v[10:11], v[2:3], 0, v[10:11]
	v_lshl_add_u64 v[12:13], v[2:3], 0, v[12:13]
	s_waitcnt vmcnt(17)
	global_store_dwordx4 v[10:11], v[72:75], off
	global_store_dwordx4 v[12:13], v[72:75], off
	v_lshl_add_u64 v[18:19], v[4:5], 0, s[4:5]
	s_add_i32 s4, s0, 3
	s_ashr_i32 s5, s4, 31
	s_lshl_b64 s[4:5], s[4:5], 11
	s_waitcnt vmcnt(18)
	global_store_dwordx4 v[10:11], v[76:79], off offset:1024
	global_store_dwordx4 v[12:13], v[76:79], off offset:1024
	s_waitcnt lgkmcnt(0)
	v_ashrrev_i32_e32 v11, 31, v14
	v_mov_b32_e32 v10, v14
	v_ashrrev_i32_e32 v13, 31, v15
	v_mov_b32_e32 v12, v15
	v_lshlrev_b64 v[10:11], 11, v[10:11]
	v_lshlrev_b64 v[12:13], 11, v[12:13]
	v_lshl_add_u64 v[10:11], v[2:3], 0, v[10:11]
	v_lshl_add_u64 v[12:13], v[2:3], 0, v[12:13]
	v_lshl_add_u64 v[14:15], v[4:5], 0, s[4:5]
	s_add_i32 s4, s1, s10
	s_ashr_i32 s5, s4, 31
	s_lshl_b64 s[4:5], s[4:5], 11
	s_lshl_b32 s1, s1, 3
	s_add_i32 s1, s1, 0
	s_waitcnt vmcnt(19)
	global_store_dwordx4 v[10:11], v[80:83], off
	global_store_dwordx4 v[12:13], v[80:83], off
	v_lshl_add_u64 v[18:19], v[4:5], 0, s[4:5]
	s_or_b32 s4, s2, 6
	s_add_i32 s2, s0, 5
	s_ashr_i32 s3, s2, 31
	s_lshl_b64 s[2:3], s[2:3], 11
	s_add_i32 s0, s0, 7
	s_waitcnt vmcnt(20)
	global_store_dwordx4 v[10:11], v[84:87], off offset:1024
	global_store_dwordx4 v[12:13], v[84:87], off offset:1024
	v_ashrrev_i32_e32 v11, 31, v16
	v_mov_b32_e32 v10, v16
	v_ashrrev_i32_e32 v13, 31, v17
	v_mov_b32_e32 v12, v17
	v_lshlrev_b64 v[10:11], 11, v[10:11]
	v_lshlrev_b64 v[12:13], 11, v[12:13]
	v_lshl_add_u64 v[10:11], v[2:3], 0, v[10:11]
	v_lshl_add_u64 v[12:13], v[2:3], 0, v[12:13]
	s_waitcnt vmcnt(21)
	global_store_dwordx4 v[10:11], v[88:91], off
	global_store_dwordx4 v[12:13], v[88:91], off
	s_waitcnt vmcnt(22)
	global_store_dwordx4 v[10:11], v[92:95], off offset:1024
	global_store_dwordx4 v[12:13], v[92:95], off offset:1024
	v_mov_b32_e32 v10, s1
	ds_read_b128 v[10:13], v10 offset:8320
	s_lshl_b32 s1, s4, 3
	s_add_i32 s1, s1, 0
	v_mov_b32_e32 v14, s1
	ds_read_b128 v[14:17], v14 offset:8320
	s_waitcnt lgkmcnt(1)
	v_ashrrev_i32_e32 v21, 31, v10
	v_mov_b32_e32 v20, v10
	v_ashrrev_i32_e32 v23, 31, v11
	v_mov_b32_e32 v22, v11
	v_lshlrev_b64 v[20:21], 11, v[20:21]
	v_lshlrev_b64 v[10:11], 11, v[22:23]
	v_lshl_add_u64 v[20:21], v[2:3], 0, v[20:21]
	v_lshl_add_u64 v[10:11], v[2:3], 0, v[10:11]
	s_ashr_i32 s1, s0, 31
	s_lshl_b64 s[0:1], s[0:1], 11
	s_waitcnt vmcnt(23)
	global_store_dwordx4 v[20:21], v[96:99], off
	global_store_dwordx4 v[10:11], v[96:99], off
	v_lshl_add_u64 v[18:19], v[4:5], 0, s[2:3]
	s_add_i32 s2, s4, s10
	s_ashr_i32 s3, s2, 31
	s_lshl_b64 s[2:3], s[2:3], 11
	s_waitcnt vmcnt(24)
	global_store_dwordx4 v[20:21], v[100:103], off offset:1024
	global_store_dwordx4 v[10:11], v[100:103], off offset:1024
	v_ashrrev_i32_e32 v11, 31, v12
	v_mov_b32_e32 v10, v12
	v_ashrrev_i32_e32 v21, 31, v13
	v_mov_b32_e32 v20, v13
	v_lshlrev_b64 v[10:11], 11, v[10:11]
	v_lshlrev_b64 v[12:13], 11, v[20:21]
	v_lshl_add_u64 v[10:11], v[2:3], 0, v[10:11]
	v_lshl_add_u64 v[12:13], v[2:3], 0, v[12:13]
	s_waitcnt vmcnt(25)
	global_store_dwordx4 v[10:11], v[104:107], off
	global_store_dwordx4 v[12:13], v[104:107], off
	v_lshl_add_u64 v[18:19], v[4:5], 0, s[2:3]
	s_waitcnt vmcnt(26)
	global_store_dwordx4 v[10:11], v[108:111], off offset:1024
	global_store_dwordx4 v[12:13], v[108:111], off offset:1024
	s_waitcnt lgkmcnt(0)
	v_ashrrev_i32_e32 v11, 31, v14
	v_mov_b32_e32 v10, v14
	v_ashrrev_i32_e32 v13, 31, v15
	v_mov_b32_e32 v12, v15
	v_lshlrev_b64 v[10:11], 11, v[10:11]
	v_lshlrev_b64 v[12:13], 11, v[12:13]
	v_lshl_add_u64 v[10:11], v[2:3], 0, v[10:11]
	v_lshl_add_u64 v[12:13], v[2:3], 0, v[12:13]
	v_lshl_add_u64 v[14:15], v[4:5], 0, s[0:1]
	s_waitcnt vmcnt(27)
	global_store_dwordx4 v[10:11], v[112:115], off
	global_store_dwordx4 v[12:13], v[112:115], off
	s_waitcnt vmcnt(28)
	global_store_dwordx4 v[10:11], v[116:119], off offset:1024
	global_store_dwordx4 v[12:13], v[116:119], off offset:1024
	s_nop 0
	v_ashrrev_i32_e32 v9, 31, v16
	v_mov_b32_e32 v8, v16
	v_ashrrev_i32_e32 v11, 31, v17
	v_mov_b32_e32 v10, v17
	v_lshlrev_b64 v[8:9], 11, v[8:9]
	v_lshlrev_b64 v[10:11], 11, v[10:11]
	v_lshl_add_u64 v[8:9], v[2:3], 0, v[8:9]
	v_lshl_add_u64 v[10:11], v[2:3], 0, v[10:11]
	s_waitcnt vmcnt(29)
	global_store_dwordx4 v[8:9], v[120:123], off
	global_store_dwordx4 v[10:11], v[120:123], off
	s_waitcnt vmcnt(30)
	global_store_dwordx4 v[8:9], v[124:127], off offset:1024
	global_store_dwordx4 v[10:11], v[124:127], off offset:1024
